# static priority raise for waves 4-7 during the FoX and SWA attention phases only (GEMM K-loops keep their per-segment toggles)
# speedup vs baseline: 1.0036x; 1.0036x over previous
; __device__ __forceinline__ int pg8_lane_id() { int l; asm volatile("v_mbcnt_lo_u32_b32 %0, -1, 0\n\tv_mbcnt_hi_u32_b32 %0, -1, %0" : "=v"(l)); return l; }
; #define LAS __attribute__((address_space(3)))
; #define REP(k) _Pragma("unroll") for (int rep_ = 0; rep_ < (((PROBE_REP_MASK >> (k)) & 1) ? 2 : 1); ++rep_)
; __device__ __forceinline__ void attn_phase(char*lds,const AttnTensors&T,const float*logft,const float*nrm,const float*b_f,__attribute__((address_space(3))) float*cumA,__attribute__((address_space(3))) float*cumB, ...
;   for(int pb=v;pb<BATCH*NHEAD*4;pb+=G){
;     const int b=pb>>6,p=(pb>>3)&7,sub=pb&7;
;     int hA,hB;
;     { const int ln_=pg8::pg8_lane_id(),hh_=ln_&15; const float bv_=b_f[hh_]; int rk=0;
;       #pragma unroll
;       for(int g=0;g<NHEAD;++g){ const float bg=__builtin_bit_cast(float,__builtin_amdgcn_readlane(__builtin_bit_cast(int,bv_),g)); rk+=(bg<bv_||(bg==bv_&&g<hh_))?1:0; }
;       const unsigned long long mA_=__ballot(rk==p&&ln_<16),mB_=__ballot(rk==15-p&&ln_<16);
;       hA=__builtin_amdgcn_readfirstlane((int)__builtin_ctzll(mA_|(1ull<<63))&15); hB=__builtin_amdgcn_readfirstlane((int)__builtin_ctzll(mB_|(1ull<<63))&15); }
;     attn_prep2(b*NHEAD+hA,b*NHEAD+hB,logft,nrm,cumA,cumB,partA,partB,wid);
;     #pragma unroll 1
;     for(int i=0;i<4;++i){ const int qb=(i==0)?sub:(i==1)?15-sub:(i==2)?7-sub:8+sub;
;       attn_unit<8>(b,(i<2)?hA:hB,qb,T.Q,T.K,T.V,T.O,lds,(lds_cfptr)((i<2)?cumA:cumB),(lds_cfptr)((i<2)?partA+48:partB+48),wid); }
; __global__ void __launch_bounds__(NWAVES * 64, 2) mk_fwd(Args args) {
;     ...
;     if (IN(3)) REP(3) {
;         static_assert(attn_body::ATTN_LDS_BYTES <= 84 * 1024, "attention scratch vs the cumulative-gate table");
;         const attn_body::AttnTensors AT{(const attn_body::bf16*)QO, (const attn_body::bf16*)KB, (const attn_body::bf16*)VB, (attn_body::bf16*)XN};
;         attn_body::attn_phase((char*)lds + RING_OFF, AT, LOGFT, (const float*)(ws + WS_NRM), args.in[8], (LAS float*)(F.lds + RING_OFF + 96 * 1024), (LAS float*)(F.lds + RING_OFF + 112 * 1024),
;                               (LAS float*)(F.lds + RING_OFF + 84 * 1024), (LAS float*)(F.lds + RING_OFF + 85 * 1024), F.vcu, F.G, F.wave);
.LBB0_371:
	s_cmp_lt_i32 s80, 4
	s_cselect_b64 s[0:1], -1, 0
	s_add_u32 s6, s78, 0x13a00000
	s_addc_u32 s7, s79, 0
	v_writelane_b32 v254, s6, 52
	s_nop 1
	v_writelane_b32 v254, s7, 53
	s_add_u32 s6, s78, 0x15a00000
	s_addc_u32 s7, s79, 0
	v_writelane_b32 v254, s6, 54
	s_and_b64 s[12:13], s[0:1], s[4:5]
	s_andn2_b64 vcc, exec, s[12:13]
	v_writelane_b32 v254, s7, 55
	s_mov_b64 s[4:5], s[76:77]
	v_writelane_b32 v254, s94, 56
	s_mov_b64 s[6:7], s[78:79]
	s_mov_b64 s[8:9], s[80:81]
	s_mov_b32 s10, s82
	v_writelane_b32 v254, s4, 57
	s_nop 1
	v_writelane_b32 v254, s5, 58
	v_writelane_b32 v254, s6, 59
	v_writelane_b32 v254, s7, 60
	v_writelane_b32 v254, s8, 61
	v_writelane_b32 v254, s9, 62
	v_writelane_b32 v255, s11, 0
	v_writelane_b32 v254, s10, 63
	v_writelane_b32 v255, s97, 1
	s_cbranch_vccnz .LBB0_584
	s_cmp_gt_u32 s96, 3
	s_cbranch_scc0 .Lmy_p3lo
	s_setprio 1
.Lmy_p3lo:
	s_lshl_b32 s0, s96, 8
	v_writelane_b32 v255, s12, 2
	s_add_i32 s51, s0, 0
	s_mul_i32 s0, s96, 0xf00
	v_writelane_b32 v255, s13, 3
	s_add_i32 s50, s51, s0
	v_writelane_b32 v255, s83, 4
	s_mov_b32 s85, s96
	s_cmpk_gt_i32 s97, 0xff
	s_mov_b32 s91, 0
	s_cbranch_scc1 .LBB0_555
	s_add_u32 s3, s78, 0x23400000
	s_addc_u32 s52, s79, 0
	s_lshl_b32 s0, s85, 2
	s_add_i32 s1, s0, 64
	s_add_i32 s5, 0, 0x15000
	s_add_i32 s4, s5, s1
	v_writelane_b32 v255, s4, 5
	s_add_i32 s4, s85, 32
	v_writelane_b32 v255, s4, 6
	s_lshl_b32 s4, s4, 2
	s_add_i32 s4, s5, s4
	s_add_i32 s1, s1, 0
	v_writelane_b32 v255, s4, 7
	s_add_i32 s1, s1, 0x15400
	v_writelane_b32 v255, s1, 8
	v_writelane_b32 v255, s5, 9
	s_add_i32 s0, s5, s0
	v_writelane_b32 v255, s0, 10
	v_readlane_b32 s0, v254, 56
	s_cmpk_gt_u32 s0, 0x7f
	s_cselect_b64 s[92:93], -1, 0
	s_cmpk_gt_u32 s0, 0xbf
	s_cselect_b64 s[94:95], -1, 0
	s_cmpk_gt_u32 s0, 0xff
	s_cselect_b64 s[96:97], -1, 0
	s_cmpk_gt_u32 s0, 0x13f
	s_cselect_b64 s[30:31], -1, 0
	s_cmpk_gt_u32 s0, 0x17f
	s_cselect_b64 s[6:7], -1, 0
	s_cmpk_gt_u32 s0, 0x1bf
	s_cselect_b64 s[4:5], -1, 0
	s_cmpk_gt_u32 s0, 0x1ff
	s_cselect_b64 s[0:1], -1, 0
	s_lshl_b32 s8, s85, 3
	s_lshl_b32 s9, s85, 4
	s_lshl_b32 s59, s85, 5
	s_and_b32 s60, s9, 48
	s_and_b32 s9, s8, 0x1fffffe0
	s_lshl_b32 s61, s85, 10
	s_cmp_lg_u32 0, -1
	s_cselect_b32 s10, 0, 0
	s_add_i32 s62, s61, s10
	s_add_i32 s10, 0, 0x15004
	v_writelane_b32 v255, s10, 11
	s_add_i32 s10, 0, 0x15008
	v_writelane_b32 v255, s10, 12
	s_add_i32 s10, 0, 0x1500c
	v_writelane_b32 v255, s10, 13
	s_add_i32 s10, 0, 0x15010
	v_writelane_b32 v255, s10, 14
	s_add_i32 s10, 0, 0x15014
	v_writelane_b32 v255, s10, 15
	s_add_i32 s10, 0, 0x15018
	v_writelane_b32 v255, s10, 16
	s_add_i32 s10, 0, 0x1501c
	v_writelane_b32 v255, s10, 17
	s_add_i32 s10, 0, 0x15080
	v_writelane_b32 v255, s10, 18
	s_add_i32 s10, 0, 0x15090
	v_writelane_b32 v255, s10, 19
	s_add_i32 s10, 0, 0x15040
	v_writelane_b32 v255, s10, 20
	s_add_i32 s10, 0, 0x15050
	v_writelane_b32 v255, s10, 21
	s_add_i32 s10, 0, 0x150c0
	v_writelane_b32 v255, s10, 22
	s_add_i32 s10, 0, 0x15404
	v_writelane_b32 v255, s10, 23
	s_add_i32 s10, 0, 0x15408
	v_writelane_b32 v255, s10, 24
	s_add_i32 s10, 0, 0x1540c
	v_writelane_b32 v255, s10, 25
	s_add_i32 s10, 0, 0x15410
	v_writelane_b32 v255, s10, 26
	s_add_i32 s10, 0, 0x15414
	v_writelane_b32 v255, s10, 27
	s_add_i32 s10, 0, 0x15418
	v_writelane_b32 v255, s10, 28
	s_add_i32 s10, 0, 0x1541c
	v_writelane_b32 v255, s10, 29
	s_add_i32 s10, 0, 0x15480
	v_writelane_b32 v255, s10, 30
	s_add_i32 s10, 0, 0x15490
	v_writelane_b32 v255, s10, 31
	s_add_i32 s10, 0, 0x15440
	v_writelane_b32 v255, s10, 32
	s_add_i32 s10, 0, 0x15450
	v_writelane_b32 v255, s10, 33
	s_add_i32 s10, 0, 0x154c0
	v_writelane_b32 v255, s10, 34
	s_mov_b32 s88, 0xfffc0000
	s_add_i32 s63, s62, 0x6000
	s_waitcnt lgkmcnt(0)
	v_mov_b32_e32 v1, 0
	v_mov_b32_e32 v188, 0xc2c80000
	s_mov_b32 s89, -1
	s_mov_b64 s[36:37], 0x20000
	s_mov_b32 s57, 0x41000000
	s_lshl_b32 s90, s8, 1
	s_lshl_b32 s44, s9, 1
	v_mov_b32_e32 v195, 0xff800000
	v_readlane_b32 s58, v255, 1
	s_branch .LBB0_375

; __device__ __forceinline__ int pg8_lane_id() { int l; asm volatile("v_mbcnt_lo_u32_b32 %0, -1, 0\n\tv_mbcnt_hi_u32_b32 %0, -1, %0" : "=v"(l)); return l; }
; #define LAS __attribute__((address_space(3)))
; __device__ __forceinline__ void swa_phase(char* lds, const bf16* Q, const bf16* K2, const bf16* V2, bf16* O, const float* sinks, const float* rel_bias, LAS float* tbl, int v, int G, const int wid) {
;     { const int lane = pg8::pg8_lane_id(), tid = wid * 64 + lane;
;       for (int i = tid; i < 16 * 256; i += NWAVES * 64) { const int hq = i >> 8, k = i & 255; tbl[i] = (k < 255) ? rel_bias[t5_bucket(k - 191) * NH + hq] * LOG2E : 0.f; } }
;     __syncthreads();
; __global__ void __launch_bounds__(NWAVES * 64, 2) mk_fwd(Args args) {
;     ...
;         if (F.G == 256 && rep_ == 0) {
;             constexpr int NODD = CONV_SWA_ODD * 128 * NWAVES; const int lo = CONV_NITEMS - CONV_SWA;
;             const int rank = F.c >> 3, xcc = F.c & 7;
;             const bool att = F.loc ? (rank < 16) : ((F.c & 1) == 0);
;             const int half = F.loc ? (xcc * 16 + (rank & 15)) : (F.c >> 1), w = half * NWAVES + F.wave;
;             const int run = F.loc ? ((xcc >> 1) * 32 + (rank & 3) * 8 + (xcc & 1) * 4 + ((rank >> 2) & 3)) : half;
;             if (att) { swa_phase((char*)lds + RING_OFF, QO, KB, VB, XN, args.in[11], args.in[13], (LAS float*)(F.lds + RING_OFF + 100 * 1024), run, 128, F.wave);
.LBB0_1359:
	s_andn2_b64 vcc, exec, s[0:1]
	s_cbranch_vccnz .LBB0_1434
	v_readlane_b32 s98, v254, 3
	s_cmp_gt_u32 s98, 3
	s_cbranch_scc0 .Lmy_p10lo
	s_setprio 1
.Lmy_p10lo:
	v_readlane_b32 s0, v254, 2
	v_mbcnt_lo_u32_b32 v1, -1, 0
	v_mbcnt_hi_u32_b32 v1, -1, v1
	s_nop 1
	v_add_u32_e32 v0, s0, v1
	s_movk_i32 s0, 0x1000
	v_cmp_gt_i32_e32 vcc, s0, v0
	s_and_saveexec_b64 s[0:1], vcc
	s_cbranch_execz .LBB0_1367
	v_lshl_add_u32 v1, v1, 2, s96
	v_add_u32_e32 v1, 0x19000, v1
	s_mov_b64 s[4:5], 0
	s_movk_i32 s12, 0xbf
	s_movk_i32 s13, 0x5a
	s_branch .LBB0_1364
